# plus: MoE GEMM loops skip the MFMAs of an expert's 128 padding slot rows (row tile 8, second half; never stored)
# baseline (speedup 1.0000x reference)
.LBB0_2360:
	s_add_u32 s2, s0, s56
	s_addc_u32 s3, s1, s57
	s_add_u32 s53, s2, 0x40200100
	s_addc_u32 s55, s3, 0
	s_add_u32 s58, s7, s56
	s_addc_u32 s59, s47, s57
	s_cmpk_eq_i32 s56, 0xf00
	s_cselect_b64 vcc, -1, 0
	s_and_b64 s[2:3], vcc, exec
	s_cselect_b32 s61, s37, s55
	s_cselect_b32 s60, s36, s53
	s_cselect_b32 s59, s51, s59
	s_cselect_b32 s58, s50, s58
	s_add_i32 s2, 0, 0x10000
	s_add_i32 s53, 0, 0x14000
	v_add_u32_e32 v170, s2, v154
	v_add_u32_e32 v187, s53, v154
	ds_read_b128 v[158:161], v170
	ds_read_b128 v[162:165], v170 offset:1024
	ds_read_b128 v[166:169], v170 offset:2048
	ds_read_b128 v[170:173], v170 offset:3072
	ds_read_b128 v[174:177], v187
	ds_read_b128 v[178:181], v187 offset:1024
	ds_read_b128 v[182:185], v187 offset:2048
	ds_read_b128 v[190:193], v187 offset:3072
	v_cndmask_b32_e32 v2, v142, v143, vcc
	v_cndmask_b32_e32 v186, v140, v155, vcc
	v_cndmask_b32_e32 v137, v138, v156, vcc
	v_cndmask_b32_e32 v139, v136, v157, vcc
	v_lshl_add_u64 v[194:195], v[146:147], 0, s[56:57]
	s_add_i32 m0, s21, 0xc000
	ds_read_b128 v[212:215], v141
	ds_read_b128 v[216:219], v141 offset:1024
	ds_read_b128 v[224:227], v141 offset:2048
	ds_read_b128 v[228:231], v141 offset:3072
	ds_read_b128 v[232:235], v141 offset:4096
	ds_read_b128 v[236:239], v141 offset:5120
	ds_read_b128 v[240:243], v141 offset:6144
	ds_read_b128 v[244:247], v141 offset:7168
	global_load_lds_dwordx4 v[194:195], off
	v_lshl_add_u64 v[194:195], v[144:145], 0, s[56:57]
	s_add_i32 m0, s21, 0xe000
	s_nop 0
	global_load_lds_dwordx4 v[194:195], off
	s_waitcnt vmcnt(8)
	s_waitcnt lgkmcnt(0)
	s_barrier
	s_setprio 1
	s_waitcnt lgkmcnt(0)
	v_mfma_f32_16x16x32_bf16 v[128:131], v[158:161], v[212:215], v[128:131]
	v_mfma_f32_16x16x32_bf16 v[124:127], v[166:169], v[212:215], v[124:127]
	v_mfma_f32_16x16x32_bf16 v[112:115], v[158:161], v[224:227], v[112:115]
	v_mfma_f32_16x16x32_bf16 v[108:111], v[166:169], v[224:227], v[108:111]
	v_mfma_f32_16x16x32_bf16 v[96:99], v[158:161], v[232:235], v[96:99]
	v_mfma_f32_16x16x32_bf16 v[92:95], v[166:169], v[232:235], v[92:95]
	v_mfma_f32_16x16x32_bf16 v[80:83], v[158:161], v[240:243], v[80:83]
	v_mfma_f32_16x16x32_bf16 v[76:79], v[166:169], v[240:243], v[76:79]
	v_mfma_f32_16x16x32_bf16 v[128:131], v[162:165], v[216:219], v[128:131]
	v_mfma_f32_16x16x32_bf16 v[124:127], v[170:173], v[216:219], v[124:127]
	v_mfma_f32_16x16x32_bf16 v[112:115], v[162:165], v[228:231], v[112:115]
	v_mfma_f32_16x16x32_bf16 v[108:111], v[170:173], v[228:231], v[108:111]
	v_mfma_f32_16x16x32_bf16 v[96:99], v[162:165], v[236:239], v[96:99]
	v_mfma_f32_16x16x32_bf16 v[92:95], v[170:173], v[236:239], v[92:95]
	v_mfma_f32_16x16x32_bf16 v[80:83], v[162:165], v[244:247], v[80:83]
	v_mfma_f32_16x16x32_bf16 v[76:79], v[170:173], v[244:247], v[76:79]
	s_setprio 0
	s_setprio 1
	v_mfma_f32_16x16x32_bf16 v[120:123], v[174:177], v[212:215], v[120:123]
	v_mfma_f32_16x16x32_bf16 v[116:119], v[182:185], v[212:215], v[116:119]
	v_mfma_f32_16x16x32_bf16 v[104:107], v[174:177], v[224:227], v[104:107]
	v_mfma_f32_16x16x32_bf16 v[100:103], v[182:185], v[224:227], v[100:103]
	v_mfma_f32_16x16x32_bf16 v[88:91], v[174:177], v[232:235], v[88:91]
	v_mfma_f32_16x16x32_bf16 v[84:87], v[182:185], v[232:235], v[84:87]
	v_mfma_f32_16x16x32_bf16 v[72:75], v[174:177], v[240:243], v[72:75]
	v_mfma_f32_16x16x32_bf16 v[68:71], v[182:185], v[240:243], v[68:71]
	v_mfma_f32_16x16x32_bf16 v[120:123], v[178:181], v[216:219], v[120:123]
	v_mfma_f32_16x16x32_bf16 v[116:119], v[190:193], v[216:219], v[116:119]
	v_mfma_f32_16x16x32_bf16 v[104:107], v[178:181], v[228:231], v[104:107]
	v_mfma_f32_16x16x32_bf16 v[100:103], v[190:193], v[228:231], v[100:103]
	v_mfma_f32_16x16x32_bf16 v[88:91], v[178:181], v[236:239], v[88:91]
	v_mfma_f32_16x16x32_bf16 v[84:87], v[190:193], v[236:239], v[84:87]
	v_mfma_f32_16x16x32_bf16 v[72:75], v[178:181], v[244:247], v[72:75]
	v_mfma_f32_16x16x32_bf16 v[68:71], v[190:193], v[244:247], v[68:71]
	s_setprio 0
	s_barrier
	s_add_i32 s2, s2, s20
	v_lshl_add_u64 v[194:195], s[58:59], 0, v[134:135]
	s_mov_b32 m0, s2
	ds_read_b128 v[212:215], v141 offset:16384
	ds_read_b128 v[216:219], v141 offset:17408
	ds_read_b128 v[224:227], v141 offset:18432
	ds_read_b128 v[228:231], v141 offset:19456
	ds_read_b128 v[232:235], v141 offset:20480
	ds_read_b128 v[236:239], v141 offset:21504
	ds_read_b128 v[240:243], v141 offset:22528
	ds_read_b128 v[244:247], v141 offset:23552
	global_load_lds_dwordx4 v[194:195], off
	s_add_i32 m0, s2, 0x2000
	s_add_u32 s2, s58, 0x80000
	v_lshl_add_u64 v[248:249], s[58:59], 0, v[132:133]
	s_addc_u32 s3, s59, 0
	s_add_i32 s53, s53, s20
	global_load_lds_dwordx4 v[248:249], off
	v_lshl_add_u64 v[250:251], s[2:3], 0, v[134:135]
	s_mov_b32 m0, s53
	v_mov_b32_e32 v187, v3
	global_load_lds_dwordx4 v[250:251], off
	v_lshl_add_u64 v[250:251], s[2:3], 0, v[132:133]
	s_add_i32 m0, s53, 0x2000
	s_nop 0
	global_load_lds_dwordx4 v[250:251], off
	s_mov_b32 m0, s21
	v_lshl_add_u64 v[250:251], s[60:61], 0, v[2:3]
	global_load_lds_dwordx4 v2, s[60:61]
	s_mov_b32 m0, s22
	s_nop 0
	global_load_lds_dwordx4 v186, s[60:61]
	s_waitcnt vmcnt(8)
	s_waitcnt lgkmcnt(0)
	v_lshl_add_u64 v[186:187], s[60:61], 0, v[186:187]
	s_barrier
	s_setprio 1
	s_waitcnt lgkmcnt(0)
	s_cmp_eq_u32 s6, 8
	s_cbranch_scc1 .Lpadskip_p8_1
	v_mfma_f32_16x16x32_bf16 v[64:67], v[158:161], v[212:215], v[64:67]
	v_mfma_f32_16x16x32_bf16 v[56:59], v[166:169], v[212:215], v[56:59]
	v_mfma_f32_16x16x32_bf16 v[48:51], v[158:161], v[224:227], v[48:51]
	v_mfma_f32_16x16x32_bf16 v[40:43], v[166:169], v[224:227], v[40:43]
	v_mfma_f32_16x16x32_bf16 v[28:31], v[158:161], v[232:235], v[28:31]
	v_mfma_f32_16x16x32_bf16 v[20:23], v[166:169], v[232:235], v[20:23]
	v_mfma_f32_16x16x32_bf16 v[12:15], v[158:161], v[240:243], v[12:15]
	v_mfma_f32_16x16x32_bf16 v[4:7], v[166:169], v[240:243], v[4:7]
	v_mfma_f32_16x16x32_bf16 v[64:67], v[162:165], v[216:219], v[64:67]
	v_mfma_f32_16x16x32_bf16 v[56:59], v[170:173], v[216:219], v[56:59]
	v_mfma_f32_16x16x32_bf16 v[48:51], v[162:165], v[228:231], v[48:51]
	v_mfma_f32_16x16x32_bf16 v[40:43], v[170:173], v[228:231], v[40:43]
	v_mfma_f32_16x16x32_bf16 v[28:31], v[162:165], v[236:239], v[28:31]
	v_mfma_f32_16x16x32_bf16 v[20:23], v[170:173], v[236:239], v[20:23]
	v_mfma_f32_16x16x32_bf16 v[12:15], v[162:165], v[244:247], v[12:15]
	v_mfma_f32_16x16x32_bf16 v[4:7], v[170:173], v[244:247], v[4:7]
	s_setprio 0
	s_setprio 1
	v_mfma_f32_16x16x32_bf16 v[60:63], v[174:177], v[212:215], v[60:63]
	v_mfma_f32_16x16x32_bf16 v[52:55], v[182:185], v[212:215], v[52:55]
	v_mfma_f32_16x16x32_bf16 v[44:47], v[174:177], v[224:227], v[44:47]
	v_mfma_f32_16x16x32_bf16 v[32:35], v[182:185], v[224:227], v[32:35]
	v_mfma_f32_16x16x32_bf16 v[36:39], v[174:177], v[232:235], v[36:39]
	v_mfma_f32_16x16x32_bf16 v[24:27], v[182:185], v[232:235], v[24:27]
	v_mfma_f32_16x16x32_bf16 v[16:19], v[174:177], v[240:243], v[16:19]
	v_mfma_f32_16x16x32_bf16 v[8:11], v[182:185], v[240:243], v[8:11]
	v_mfma_f32_16x16x32_bf16 v[60:63], v[178:181], v[216:219], v[60:63]
	v_mfma_f32_16x16x32_bf16 v[52:55], v[190:193], v[216:219], v[52:55]
	v_mfma_f32_16x16x32_bf16 v[44:47], v[178:181], v[228:231], v[44:47]
	v_mfma_f32_16x16x32_bf16 v[32:35], v[190:193], v[228:231], v[32:35]
	v_mfma_f32_16x16x32_bf16 v[36:39], v[178:181], v[236:239], v[36:39]
	v_mfma_f32_16x16x32_bf16 v[24:27], v[190:193], v[236:239], v[24:27]
	v_mfma_f32_16x16x32_bf16 v[16:19], v[178:181], v[244:247], v[16:19]
	v_mfma_f32_16x16x32_bf16 v[8:11], v[190:193], v[244:247], v[8:11]
.Lpadskip_p8_1:
	s_setprio 0
	s_barrier
	s_add_i32 s2, 0, 0x18000
	v_add_u32_e32 v2, s2, v154
	s_add_i32 s53, 0, 0x1c000
	ds_read_b128 v[158:161], v2
	ds_read_b128 v[162:165], v2 offset:1024
	ds_read_b128 v[166:169], v2 offset:2048
	ds_read_b128 v[170:173], v2 offset:3072
	v_add_u32_e32 v2, s53, v154
	ds_read_b128 v[174:177], v2
	ds_read_b128 v[178:181], v2 offset:1024
	ds_read_b128 v[182:185], v2 offset:2048
	ds_read_b128 v[190:193], v2 offset:3072
	s_mov_b32 m0, s23
	ds_read_b128 v[212:215], v141 offset:32768
	ds_read_b128 v[216:219], v141 offset:33792
	ds_read_b128 v[224:227], v141 offset:34816
	ds_read_b128 v[228:231], v141 offset:35840
	ds_read_b128 v[232:235], v141 offset:36864
	ds_read_b128 v[236:239], v141 offset:37888
	ds_read_b128 v[240:243], v141 offset:38912
	ds_read_b128 v[244:247], v141 offset:39936
	global_load_lds_dwordx4 v137, s[60:61]
	s_mov_b32 m0, s24
	s_nop 0
	global_load_lds_dwordx4 v139, s[60:61]
	s_waitcnt vmcnt(8)
	s_waitcnt lgkmcnt(0)
	s_barrier
	s_setprio 1
	s_waitcnt lgkmcnt(0)
	v_mfma_f32_16x16x32_bf16 v[128:131], v[158:161], v[212:215], v[128:131]
	v_mfma_f32_16x16x32_bf16 v[124:127], v[166:169], v[212:215], v[124:127]
	v_mfma_f32_16x16x32_bf16 v[112:115], v[158:161], v[224:227], v[112:115]
	v_mfma_f32_16x16x32_bf16 v[108:111], v[166:169], v[224:227], v[108:111]
	v_mfma_f32_16x16x32_bf16 v[96:99], v[158:161], v[232:235], v[96:99]
	v_mfma_f32_16x16x32_bf16 v[92:95], v[166:169], v[232:235], v[92:95]
	v_mfma_f32_16x16x32_bf16 v[80:83], v[158:161], v[240:243], v[80:83]
	v_mfma_f32_16x16x32_bf16 v[76:79], v[166:169], v[240:243], v[76:79]
	v_mfma_f32_16x16x32_bf16 v[128:131], v[162:165], v[216:219], v[128:131]
	v_mfma_f32_16x16x32_bf16 v[124:127], v[170:173], v[216:219], v[124:127]
	v_mfma_f32_16x16x32_bf16 v[112:115], v[162:165], v[228:231], v[112:115]
	v_mfma_f32_16x16x32_bf16 v[108:111], v[170:173], v[228:231], v[108:111]
	v_mfma_f32_16x16x32_bf16 v[96:99], v[162:165], v[236:239], v[96:99]
	v_mfma_f32_16x16x32_bf16 v[92:95], v[170:173], v[236:239], v[92:95]
	v_mfma_f32_16x16x32_bf16 v[80:83], v[162:165], v[244:247], v[80:83]
	v_mfma_f32_16x16x32_bf16 v[76:79], v[170:173], v[244:247], v[76:79]
	s_setprio 0
	s_setprio 1
	v_mfma_f32_16x16x32_bf16 v[120:123], v[174:177], v[212:215], v[120:123]
	v_mfma_f32_16x16x32_bf16 v[116:119], v[182:185], v[212:215], v[116:119]
	v_mfma_f32_16x16x32_bf16 v[104:107], v[174:177], v[224:227], v[104:107]
	v_mfma_f32_16x16x32_bf16 v[100:103], v[182:185], v[224:227], v[100:103]
	v_mfma_f32_16x16x32_bf16 v[88:91], v[174:177], v[232:235], v[88:91]
	v_mfma_f32_16x16x32_bf16 v[84:87], v[182:185], v[232:235], v[84:87]
	v_mfma_f32_16x16x32_bf16 v[72:75], v[174:177], v[240:243], v[72:75]
	v_mfma_f32_16x16x32_bf16 v[68:71], v[182:185], v[240:243], v[68:71]
	v_mfma_f32_16x16x32_bf16 v[120:123], v[178:181], v[216:219], v[120:123]
	v_mfma_f32_16x16x32_bf16 v[116:119], v[190:193], v[216:219], v[116:119]
	v_mfma_f32_16x16x32_bf16 v[104:107], v[178:181], v[228:231], v[104:107]
	v_mfma_f32_16x16x32_bf16 v[100:103], v[190:193], v[228:231], v[100:103]
	v_mfma_f32_16x16x32_bf16 v[88:91], v[178:181], v[236:239], v[88:91]
	v_mfma_f32_16x16x32_bf16 v[84:87], v[190:193], v[236:239], v[84:87]
	v_mfma_f32_16x16x32_bf16 v[72:75], v[178:181], v[244:247], v[72:75]
	v_mfma_f32_16x16x32_bf16 v[68:71], v[190:193], v[244:247], v[68:71]
	s_setprio 0
	s_barrier
	s_add_i32 s2, s2, s20
	v_lshl_add_u64 v[194:195], v[194:195], 0, s[30:31]
	s_mov_b32 m0, s2
	ds_read_b128 v[212:215], v141 offset:49152
	ds_read_b128 v[216:219], v141 offset:50176
	ds_read_b128 v[224:227], v141 offset:51200
	ds_read_b128 v[228:231], v141 offset:52224
	ds_read_b128 v[232:235], v141 offset:53248
	ds_read_b128 v[236:239], v141 offset:54272
	ds_read_b128 v[240:243], v141 offset:55296
	ds_read_b128 v[244:247], v141 offset:56320
	global_load_lds_dwordx4 v[194:195], off
	s_add_i32 m0, s2, 0x2000
	s_add_u32 s2, s58, 0x80080
	v_lshl_add_u64 v[194:195], v[248:249], 0, s[30:31]
	s_addc_u32 s3, s59, 0
	s_add_i32 s53, s53, s20
	global_load_lds_dwordx4 v[194:195], off
	v_lshl_add_u64 v[194:195], s[2:3], 0, v[134:135]
	s_mov_b32 m0, s53
	v_lshl_add_u64 v[186:187], v[186:187], 0, s[30:31]
	global_load_lds_dwordx4 v[194:195], off
	v_lshl_add_u64 v[194:195], s[2:3], 0, v[132:133]
	s_add_i32 m0, s53, 0x2000
	s_nop 0
	global_load_lds_dwordx4 v[194:195], off
	v_lshl_add_u64 v[194:195], v[250:251], 0, s[30:31]
	s_mov_b32 m0, s26
	s_nop 0
	global_load_lds_dwordx4 v[194:195], off
	s_mov_b32 m0, s27
	s_nop 0
	global_load_lds_dwordx4 v[186:187], off
	s_waitcnt vmcnt(8)
	s_waitcnt lgkmcnt(0)
	s_barrier
	s_setprio 1
	s_waitcnt lgkmcnt(0)
	s_cmp_eq_u32 s6, 8
	s_cbranch_scc1 .Lpadskip_p8_3
	v_mfma_f32_16x16x32_bf16 v[64:67], v[158:161], v[212:215], v[64:67]
	v_mfma_f32_16x16x32_bf16 v[56:59], v[166:169], v[212:215], v[56:59]
	v_mfma_f32_16x16x32_bf16 v[48:51], v[158:161], v[224:227], v[48:51]
	v_mfma_f32_16x16x32_bf16 v[40:43], v[166:169], v[224:227], v[40:43]
	v_mfma_f32_16x16x32_bf16 v[28:31], v[158:161], v[232:235], v[28:31]
	v_mfma_f32_16x16x32_bf16 v[20:23], v[166:169], v[232:235], v[20:23]
	v_mfma_f32_16x16x32_bf16 v[12:15], v[158:161], v[240:243], v[12:15]
	v_mfma_f32_16x16x32_bf16 v[4:7], v[166:169], v[240:243], v[4:7]
	v_mfma_f32_16x16x32_bf16 v[64:67], v[162:165], v[216:219], v[64:67]
	v_mfma_f32_16x16x32_bf16 v[56:59], v[170:173], v[216:219], v[56:59]
	v_mfma_f32_16x16x32_bf16 v[48:51], v[162:165], v[228:231], v[48:51]
	v_mfma_f32_16x16x32_bf16 v[40:43], v[170:173], v[228:231], v[40:43]
	v_mfma_f32_16x16x32_bf16 v[28:31], v[162:165], v[236:239], v[28:31]
	v_mfma_f32_16x16x32_bf16 v[20:23], v[170:173], v[236:239], v[20:23]
	v_mfma_f32_16x16x32_bf16 v[12:15], v[162:165], v[244:247], v[12:15]
	v_mfma_f32_16x16x32_bf16 v[4:7], v[170:173], v[244:247], v[4:7]
	s_setprio 0
	s_setprio 1
	v_mfma_f32_16x16x32_bf16 v[60:63], v[174:177], v[212:215], v[60:63]
	v_mfma_f32_16x16x32_bf16 v[52:55], v[182:185], v[212:215], v[52:55]
	v_mfma_f32_16x16x32_bf16 v[44:47], v[174:177], v[224:227], v[44:47]
	v_mfma_f32_16x16x32_bf16 v[32:35], v[182:185], v[224:227], v[32:35]
	v_mfma_f32_16x16x32_bf16 v[36:39], v[174:177], v[232:235], v[36:39]
	v_mfma_f32_16x16x32_bf16 v[24:27], v[182:185], v[232:235], v[24:27]
	v_mfma_f32_16x16x32_bf16 v[16:19], v[174:177], v[240:243], v[16:19]
	v_mfma_f32_16x16x32_bf16 v[8:11], v[182:185], v[240:243], v[8:11]
	v_mfma_f32_16x16x32_bf16 v[60:63], v[178:181], v[216:219], v[60:63]
	v_mfma_f32_16x16x32_bf16 v[52:55], v[190:193], v[216:219], v[52:55]
	v_mfma_f32_16x16x32_bf16 v[44:47], v[178:181], v[228:231], v[44:47]
	v_mfma_f32_16x16x32_bf16 v[32:35], v[190:193], v[228:231], v[32:35]
	v_mfma_f32_16x16x32_bf16 v[36:39], v[178:181], v[236:239], v[36:39]
	v_mfma_f32_16x16x32_bf16 v[24:27], v[190:193], v[236:239], v[24:27]
	v_mfma_f32_16x16x32_bf16 v[16:19], v[178:181], v[244:247], v[16:19]
	v_mfma_f32_16x16x32_bf16 v[8:11], v[190:193], v[244:247], v[8:11]
.Lpadskip_p8_3:
	s_setprio 0
	s_barrier
	s_add_i32 s49, s49, 2
	s_add_u32 s56, s56, 0x100
	s_addc_u32 s57, s57, 0
	s_cmp_gt_u32 s49, 29
	s_cbranch_scc0 .LBB0_2360
	s_and_b64 vcc, exec, s[44:45]
	s_cbranch_vccz .LBB0_2363
	s_barrier

.LBB0_2430:
	s_add_u32 s2, s56, 0x80
	s_addc_u32 s3, s57, 0
	s_cmp_eq_u32 s41, 28
	s_cselect_b32 s61, s51, s3
	s_cselect_b32 s60, s50, s2
	s_cselect_b32 s59, s55, s7
	s_cselect_b32 s58, s54, s6
	s_add_i32 s2, 0, 0x10000
	v_add_u32_e32 v146, s2, v150
	s_add_i32 s43, 0, 0x14000
	ds_read_b128 v[152:155], v146
	ds_read_b128 v[156:159], v146 offset:1024
	ds_read_b128 v[160:163], v146 offset:2048
	ds_read_b128 v[164:167], v146 offset:3072
	v_add_u32_e32 v146, s43, v150
	ds_read_b128 v[168:171], v146
	ds_read_b128 v[172:175], v146 offset:1024
	ds_read_b128 v[176:179], v146 offset:2048
	ds_read_b128 v[180:183], v146 offset:3072
	v_lshl_add_u64 v[146:147], s[56:57], 0, v[144:145]
	s_add_i32 m0, s23, 0xc000
	ds_read_b128 v[184:187], v151
	ds_read_b128 v[190:193], v151 offset:1024
	ds_read_b128 v[212:215], v151 offset:2048
	ds_read_b128 v[216:219], v151 offset:3072
	ds_read_b128 v[224:227], v151 offset:4096
	ds_read_b128 v[228:231], v151 offset:5120
	ds_read_b128 v[232:235], v151 offset:6144
	ds_read_b128 v[236:239], v151 offset:7168
	global_load_lds_dwordx4 v[146:147], off
	v_lshl_add_u64 v[146:147], s[56:57], 0, v[142:143]
	s_add_i32 m0, s23, 0xe000
	s_nop 0
	global_load_lds_dwordx4 v[146:147], off
	s_waitcnt vmcnt(8)
	s_waitcnt lgkmcnt(0)
	s_barrier
	s_setprio 1
	s_waitcnt lgkmcnt(0)
	v_mfma_f32_16x16x32_bf16 v[128:131], v[152:155], v[184:187], v[128:131]
	v_mfma_f32_16x16x32_bf16 v[124:127], v[160:163], v[184:187], v[124:127]
	v_mfma_f32_16x16x32_bf16 v[120:123], v[152:155], v[212:215], v[120:123]
	v_mfma_f32_16x16x32_bf16 v[116:119], v[160:163], v[212:215], v[116:119]
	v_mfma_f32_16x16x32_bf16 v[104:107], v[152:155], v[224:227], v[104:107]
	v_mfma_f32_16x16x32_bf16 v[100:103], v[160:163], v[224:227], v[100:103]
	v_mfma_f32_16x16x32_bf16 v[88:91], v[152:155], v[232:235], v[88:91]
	v_mfma_f32_16x16x32_bf16 v[84:87], v[160:163], v[232:235], v[84:87]
	v_mfma_f32_16x16x32_bf16 v[128:131], v[156:159], v[190:193], v[128:131]
	v_mfma_f32_16x16x32_bf16 v[124:127], v[164:167], v[190:193], v[124:127]
	v_mfma_f32_16x16x32_bf16 v[120:123], v[156:159], v[216:219], v[120:123]
	v_mfma_f32_16x16x32_bf16 v[116:119], v[164:167], v[216:219], v[116:119]
	v_mfma_f32_16x16x32_bf16 v[104:107], v[156:159], v[228:231], v[104:107]
	v_mfma_f32_16x16x32_bf16 v[100:103], v[164:167], v[228:231], v[100:103]
	v_mfma_f32_16x16x32_bf16 v[88:91], v[156:159], v[236:239], v[88:91]
	v_mfma_f32_16x16x32_bf16 v[84:87], v[164:167], v[236:239], v[84:87]
	s_setprio 0
	s_setprio 1
	v_mfma_f32_16x16x32_bf16 v[112:115], v[168:171], v[184:187], v[112:115]
	v_mfma_f32_16x16x32_bf16 v[108:111], v[176:179], v[184:187], v[108:111]
	v_mfma_f32_16x16x32_bf16 v[96:99], v[168:171], v[212:215], v[96:99]
	v_mfma_f32_16x16x32_bf16 v[92:95], v[176:179], v[212:215], v[92:95]
	v_mfma_f32_16x16x32_bf16 v[80:83], v[168:171], v[224:227], v[80:83]
	v_mfma_f32_16x16x32_bf16 v[72:75], v[176:179], v[224:227], v[72:75]
	v_mfma_f32_16x16x32_bf16 v[56:59], v[168:171], v[232:235], v[56:59]
	v_mfma_f32_16x16x32_bf16 v[52:55], v[176:179], v[232:235], v[52:55]
	v_mfma_f32_16x16x32_bf16 v[112:115], v[172:175], v[190:193], v[112:115]
	v_mfma_f32_16x16x32_bf16 v[108:111], v[180:183], v[190:193], v[108:111]
	v_mfma_f32_16x16x32_bf16 v[96:99], v[172:175], v[216:219], v[96:99]
	v_mfma_f32_16x16x32_bf16 v[92:95], v[180:183], v[216:219], v[92:95]
	v_mfma_f32_16x16x32_bf16 v[80:83], v[172:175], v[228:231], v[80:83]
	v_mfma_f32_16x16x32_bf16 v[72:75], v[180:183], v[228:231], v[72:75]
	v_mfma_f32_16x16x32_bf16 v[56:59], v[172:175], v[236:239], v[56:59]
	v_mfma_f32_16x16x32_bf16 v[52:55], v[180:183], v[236:239], v[52:55]
	s_setprio 0
	s_barrier
	s_add_i32 s2, s2, s21
	v_lshl_add_u64 v[146:147], s[58:59], 0, v[2:3]
	s_mov_b32 m0, s2
	ds_read_b128 v[184:187], v151 offset:16384
	ds_read_b128 v[190:193], v151 offset:17408
	ds_read_b128 v[212:215], v151 offset:18432
	ds_read_b128 v[216:219], v151 offset:19456
	ds_read_b128 v[224:227], v151 offset:20480
	ds_read_b128 v[228:231], v151 offset:21504
	ds_read_b128 v[232:235], v151 offset:22528
	ds_read_b128 v[236:239], v151 offset:23552
	global_load_lds_dwordx4 v[146:147], off
	s_add_i32 m0, s2, 0x2000
	s_add_u32 s2, s58, 0x80000
	v_lshl_add_u64 v[194:195], s[58:59], 0, v[132:133]
	s_addc_u32 s3, s59, 0
	s_add_i32 s43, s43, s21
	global_load_lds_dwordx4 v[194:195], off
	v_lshl_add_u64 v[240:241], s[2:3], 0, v[2:3]
	s_mov_b32 m0, s43
	v_lshl_add_u64 v[242:243], s[60:61], 0, v[136:137]
	global_load_lds_dwordx4 v[240:241], off
	v_lshl_add_u64 v[240:241], s[2:3], 0, v[132:133]
	s_add_i32 m0, s43, 0x2000
	s_nop 0
	global_load_lds_dwordx4 v[240:241], off
	v_lshl_add_u64 v[240:241], s[60:61], 0, v[134:135]
	s_mov_b32 m0, s23
	s_nop 0
	global_load_lds_dwordx4 v[240:241], off
	s_mov_b32 m0, s24
	s_nop 0
	global_load_lds_dwordx4 v[242:243], off
	s_waitcnt vmcnt(8)
	s_waitcnt lgkmcnt(0)
	s_barrier
	s_setprio 1
	s_waitcnt lgkmcnt(0)
	s_cmp_eq_u32 s36, 8
	s_cbranch_scc1 .Lpadskip_p9_1
	v_mfma_f32_16x16x32_bf16 v[36:39], v[152:155], v[184:187], v[36:39]
	v_mfma_f32_16x16x32_bf16 v[28:31], v[160:163], v[184:187], v[28:31]
	v_mfma_f32_16x16x32_bf16 v[24:27], v[152:155], v[212:215], v[24:27]
	v_mfma_f32_16x16x32_bf16 v[20:23], v[160:163], v[212:215], v[20:23]
	v_mfma_f32_16x16x32_bf16 v[16:19], v[152:155], v[224:227], v[16:19]
	v_mfma_f32_16x16x32_bf16 v[12:15], v[160:163], v[224:227], v[12:15]
	v_mfma_f32_16x16x32_bf16 v[8:11], v[152:155], v[232:235], v[8:11]
	v_mfma_f32_16x16x32_bf16 v[4:7], v[160:163], v[232:235], v[4:7]
	v_mfma_f32_16x16x32_bf16 v[36:39], v[156:159], v[190:193], v[36:39]
	v_mfma_f32_16x16x32_bf16 v[28:31], v[164:167], v[190:193], v[28:31]
	v_mfma_f32_16x16x32_bf16 v[24:27], v[156:159], v[216:219], v[24:27]
	v_mfma_f32_16x16x32_bf16 v[20:23], v[164:167], v[216:219], v[20:23]
	v_mfma_f32_16x16x32_bf16 v[16:19], v[156:159], v[228:231], v[16:19]
	v_mfma_f32_16x16x32_bf16 v[12:15], v[164:167], v[228:231], v[12:15]
	v_mfma_f32_16x16x32_bf16 v[8:11], v[156:159], v[236:239], v[8:11]
	v_mfma_f32_16x16x32_bf16 v[4:7], v[164:167], v[236:239], v[4:7]
	s_setprio 0
	s_setprio 1
	v_mfma_f32_16x16x32_bf16 v[68:71], v[168:171], v[184:187], v[68:71]
	v_mfma_f32_16x16x32_bf16 v[76:79], v[176:179], v[184:187], v[76:79]
	v_mfma_f32_16x16x32_bf16 v[60:63], v[168:171], v[212:215], v[60:63]
	v_mfma_f32_16x16x32_bf16 v[64:67], v[176:179], v[212:215], v[64:67]
	v_mfma_f32_16x16x32_bf16 v[44:47], v[168:171], v[224:227], v[44:47]
	v_mfma_f32_16x16x32_bf16 v[48:51], v[176:179], v[224:227], v[48:51]
	v_mfma_f32_16x16x32_bf16 v[32:35], v[168:171], v[232:235], v[32:35]
	v_mfma_f32_16x16x32_bf16 v[40:43], v[176:179], v[232:235], v[40:43]
	v_mfma_f32_16x16x32_bf16 v[68:71], v[172:175], v[190:193], v[68:71]
	v_mfma_f32_16x16x32_bf16 v[76:79], v[180:183], v[190:193], v[76:79]
	v_mfma_f32_16x16x32_bf16 v[60:63], v[172:175], v[216:219], v[60:63]
	v_mfma_f32_16x16x32_bf16 v[64:67], v[180:183], v[216:219], v[64:67]
	v_mfma_f32_16x16x32_bf16 v[44:47], v[172:175], v[228:231], v[44:47]
	v_mfma_f32_16x16x32_bf16 v[48:51], v[180:183], v[228:231], v[48:51]
	v_mfma_f32_16x16x32_bf16 v[32:35], v[172:175], v[236:239], v[32:35]
	v_mfma_f32_16x16x32_bf16 v[40:43], v[180:183], v[236:239], v[40:43]
.Lpadskip_p9_1:
	s_setprio 0
	s_barrier
	s_add_i32 s2, 0, 0x18000
	s_add_i32 s43, 0, 0x1c000
	v_add_u32_e32 v164, s2, v150
	v_add_u32_e32 v180, s43, v150
	ds_read_b128 v[152:155], v164
	ds_read_b128 v[156:159], v164 offset:1024
	ds_read_b128 v[160:163], v164 offset:2048
	ds_read_b128 v[164:167], v164 offset:3072
	ds_read_b128 v[168:171], v180
	ds_read_b128 v[172:175], v180 offset:1024
	ds_read_b128 v[176:179], v180 offset:2048
	ds_read_b128 v[180:183], v180 offset:3072
	s_mov_b32 m0, s25
	v_lshl_add_u64 v[244:245], s[60:61], 0, v[138:139]
	ds_read_b128 v[184:187], v151 offset:32768
	ds_read_b128 v[190:193], v151 offset:33792
	ds_read_b128 v[212:215], v151 offset:34816
	ds_read_b128 v[216:219], v151 offset:35840
	ds_read_b128 v[224:227], v151 offset:36864
	ds_read_b128 v[228:231], v151 offset:37888
	ds_read_b128 v[232:235], v151 offset:38912
	ds_read_b128 v[236:239], v151 offset:39936
	global_load_lds_dwordx4 v[244:245], off
	v_lshl_add_u64 v[244:245], s[60:61], 0, v[140:141]
	s_mov_b32 m0, s26
	s_nop 0
	global_load_lds_dwordx4 v[244:245], off
	s_waitcnt vmcnt(8)
	s_waitcnt lgkmcnt(0)
	s_barrier
	s_setprio 1
	s_waitcnt lgkmcnt(0)
	v_mfma_f32_16x16x32_bf16 v[128:131], v[152:155], v[184:187], v[128:131]
	v_mfma_f32_16x16x32_bf16 v[124:127], v[160:163], v[184:187], v[124:127]
	v_mfma_f32_16x16x32_bf16 v[120:123], v[152:155], v[212:215], v[120:123]
	v_mfma_f32_16x16x32_bf16 v[116:119], v[160:163], v[212:215], v[116:119]
	v_mfma_f32_16x16x32_bf16 v[104:107], v[152:155], v[224:227], v[104:107]
	v_mfma_f32_16x16x32_bf16 v[100:103], v[160:163], v[224:227], v[100:103]
	v_mfma_f32_16x16x32_bf16 v[88:91], v[152:155], v[232:235], v[88:91]
	v_mfma_f32_16x16x32_bf16 v[84:87], v[160:163], v[232:235], v[84:87]
	v_mfma_f32_16x16x32_bf16 v[128:131], v[156:159], v[190:193], v[128:131]
	v_mfma_f32_16x16x32_bf16 v[124:127], v[164:167], v[190:193], v[124:127]
	v_mfma_f32_16x16x32_bf16 v[120:123], v[156:159], v[216:219], v[120:123]
	v_mfma_f32_16x16x32_bf16 v[116:119], v[164:167], v[216:219], v[116:119]
	v_mfma_f32_16x16x32_bf16 v[104:107], v[156:159], v[228:231], v[104:107]
	v_mfma_f32_16x16x32_bf16 v[100:103], v[164:167], v[228:231], v[100:103]
	v_mfma_f32_16x16x32_bf16 v[88:91], v[156:159], v[236:239], v[88:91]
	v_mfma_f32_16x16x32_bf16 v[84:87], v[164:167], v[236:239], v[84:87]
	s_setprio 0
	s_setprio 1
	v_mfma_f32_16x16x32_bf16 v[112:115], v[168:171], v[184:187], v[112:115]
	v_mfma_f32_16x16x32_bf16 v[108:111], v[176:179], v[184:187], v[108:111]
	v_mfma_f32_16x16x32_bf16 v[96:99], v[168:171], v[212:215], v[96:99]
	v_mfma_f32_16x16x32_bf16 v[92:95], v[176:179], v[212:215], v[92:95]
	v_mfma_f32_16x16x32_bf16 v[80:83], v[168:171], v[224:227], v[80:83]
	v_mfma_f32_16x16x32_bf16 v[72:75], v[176:179], v[224:227], v[72:75]
	v_mfma_f32_16x16x32_bf16 v[56:59], v[168:171], v[232:235], v[56:59]
	v_mfma_f32_16x16x32_bf16 v[52:55], v[176:179], v[232:235], v[52:55]
	v_mfma_f32_16x16x32_bf16 v[112:115], v[172:175], v[190:193], v[112:115]
	v_mfma_f32_16x16x32_bf16 v[108:111], v[180:183], v[190:193], v[108:111]
	v_mfma_f32_16x16x32_bf16 v[96:99], v[172:175], v[216:219], v[96:99]
	v_mfma_f32_16x16x32_bf16 v[92:95], v[180:183], v[216:219], v[92:95]
	v_mfma_f32_16x16x32_bf16 v[80:83], v[172:175], v[228:231], v[80:83]
	v_mfma_f32_16x16x32_bf16 v[72:75], v[180:183], v[228:231], v[72:75]
	v_mfma_f32_16x16x32_bf16 v[56:59], v[172:175], v[236:239], v[56:59]
	v_mfma_f32_16x16x32_bf16 v[52:55], v[180:183], v[236:239], v[52:55]
	s_setprio 0
	s_barrier
	s_add_i32 s2, s2, s21
	v_lshl_add_u64 v[146:147], v[146:147], 0, s[30:31]
	s_mov_b32 m0, s2
	ds_read_b128 v[184:187], v151 offset:49152
	ds_read_b128 v[190:193], v151 offset:50176
	ds_read_b128 v[212:215], v151 offset:51200
	ds_read_b128 v[216:219], v151 offset:52224
	ds_read_b128 v[224:227], v151 offset:53248
	ds_read_b128 v[228:231], v151 offset:54272
	ds_read_b128 v[232:235], v151 offset:55296
	ds_read_b128 v[236:239], v151 offset:56320
	global_load_lds_dwordx4 v[146:147], off
	s_add_i32 m0, s2, 0x2000
	s_add_u32 s2, s58, 0x80080
	v_lshl_add_u64 v[146:147], v[194:195], 0, s[30:31]
	s_addc_u32 s3, s59, 0
	s_add_i32 s43, s43, s21
	global_load_lds_dwordx4 v[146:147], off
	v_lshl_add_u64 v[146:147], s[2:3], 0, v[2:3]
	s_mov_b32 m0, s43
	s_nop 0
	global_load_lds_dwordx4 v[146:147], off
	v_lshl_add_u64 v[146:147], s[2:3], 0, v[132:133]
	s_add_i32 m0, s43, 0x2000
	s_nop 0
	global_load_lds_dwordx4 v[146:147], off
	v_lshl_add_u64 v[146:147], v[240:241], 0, s[30:31]
	s_mov_b32 m0, s28
	s_nop 0
	global_load_lds_dwordx4 v[146:147], off
	v_lshl_add_u64 v[146:147], v[242:243], 0, s[30:31]
	s_mov_b32 m0, s29
	s_nop 0
	global_load_lds_dwordx4 v[146:147], off
	s_waitcnt vmcnt(8)
	s_waitcnt lgkmcnt(0)
	s_barrier
	s_setprio 1
	s_waitcnt lgkmcnt(0)
	s_cmp_eq_u32 s36, 8
	s_cbranch_scc1 .Lpadskip_p9_3
	v_mfma_f32_16x16x32_bf16 v[36:39], v[152:155], v[184:187], v[36:39]
	v_mfma_f32_16x16x32_bf16 v[28:31], v[160:163], v[184:187], v[28:31]
	v_mfma_f32_16x16x32_bf16 v[24:27], v[152:155], v[212:215], v[24:27]
	v_mfma_f32_16x16x32_bf16 v[20:23], v[160:163], v[212:215], v[20:23]
	v_mfma_f32_16x16x32_bf16 v[16:19], v[152:155], v[224:227], v[16:19]
	v_mfma_f32_16x16x32_bf16 v[12:15], v[160:163], v[224:227], v[12:15]
	v_mfma_f32_16x16x32_bf16 v[8:11], v[152:155], v[232:235], v[8:11]
	v_mfma_f32_16x16x32_bf16 v[4:7], v[160:163], v[232:235], v[4:7]
	v_mfma_f32_16x16x32_bf16 v[36:39], v[156:159], v[190:193], v[36:39]
	v_mfma_f32_16x16x32_bf16 v[28:31], v[164:167], v[190:193], v[28:31]
	v_mfma_f32_16x16x32_bf16 v[24:27], v[156:159], v[216:219], v[24:27]
	v_mfma_f32_16x16x32_bf16 v[20:23], v[164:167], v[216:219], v[20:23]
	v_mfma_f32_16x16x32_bf16 v[16:19], v[156:159], v[228:231], v[16:19]
	v_mfma_f32_16x16x32_bf16 v[12:15], v[164:167], v[228:231], v[12:15]
	v_mfma_f32_16x16x32_bf16 v[8:11], v[156:159], v[236:239], v[8:11]
	v_mfma_f32_16x16x32_bf16 v[4:7], v[164:167], v[236:239], v[4:7]
	s_setprio 0
	s_setprio 1
	v_mfma_f32_16x16x32_bf16 v[68:71], v[168:171], v[184:187], v[68:71]
	v_mfma_f32_16x16x32_bf16 v[76:79], v[176:179], v[184:187], v[76:79]
	v_mfma_f32_16x16x32_bf16 v[60:63], v[168:171], v[212:215], v[60:63]
	v_mfma_f32_16x16x32_bf16 v[64:67], v[176:179], v[212:215], v[64:67]
	v_mfma_f32_16x16x32_bf16 v[44:47], v[168:171], v[224:227], v[44:47]
	v_mfma_f32_16x16x32_bf16 v[48:51], v[176:179], v[224:227], v[48:51]
	v_mfma_f32_16x16x32_bf16 v[32:35], v[168:171], v[232:235], v[32:35]
	v_mfma_f32_16x16x32_bf16 v[40:43], v[176:179], v[232:235], v[40:43]
	v_mfma_f32_16x16x32_bf16 v[68:71], v[172:175], v[190:193], v[68:71]
	v_mfma_f32_16x16x32_bf16 v[76:79], v[180:183], v[190:193], v[76:79]
	v_mfma_f32_16x16x32_bf16 v[60:63], v[172:175], v[216:219], v[60:63]
	v_mfma_f32_16x16x32_bf16 v[64:67], v[180:183], v[216:219], v[64:67]
	v_mfma_f32_16x16x32_bf16 v[44:47], v[172:175], v[228:231], v[44:47]
	v_mfma_f32_16x16x32_bf16 v[48:51], v[180:183], v[228:231], v[48:51]
	v_mfma_f32_16x16x32_bf16 v[32:35], v[172:175], v[236:239], v[32:35]
	v_mfma_f32_16x16x32_bf16 v[40:43], v[180:183], v[236:239], v[40:43]
.Lpadskip_p9_3:
	s_setprio 0
	s_barrier
	s_add_i32 s41, s41, 2
	s_add_u32 s56, s56, 0x100
	s_addc_u32 s57, s57, 0
	s_add_u32 s6, s6, 0x100
	s_addc_u32 s7, s7, 0
	s_cmp_gt_u32 s41, 29
	s_cbranch_scc0 .LBB0_2430
	s_and_b64 vcc, exec, s[38:39]
	s_cbranch_vccz .LBB0_2433
	s_barrier
